# baseline (speedup 1.0000x reference)
.LBB1_235:
	v_subrev_u32_e32 v0, 0x100, v0
	s_movk_i32 s0, 0xf0
	v_cmp_gt_u32_e32 vcc, s0, v0
	s_and_saveexec_b64 s[0:1], vcc
	s_cbranch_execz .Lepi_idle
	s_load_dwordx4 s[68:71], s[14:15], 0x0
	s_load_dwordx2 s[72:73], s[14:15], 0x10
	s_movk_i32 s0, 0x77
	v_mov_b32_e32 v1, 0xffffff88
	v_cmp_lt_u32_e32 vcc, s0, v0
	v_mov_b32_e32 v2, 0x44704000
	s_mov_b32 s0, 0xf800000
	v_cndmask_b32_e32 v1, 0, v1, vcc
	v_add_u32_e32 v0, v1, v0
	v_cvt_f32_u32_e32 v1, v0
	s_mov_b32 s5, 0x17800
	s_mov_b32 s4, 0x3eb17218
	v_fmac_f32_e32 v2, 0xc1000000, v1
	v_mul_f32_e32 v1, 0x4f800000, v2
	v_cmp_gt_f32_e64 s[0:1], s0, v2
	s_nop 1
	v_cndmask_b32_e64 v1, v2, v1, s[0:1]
	v_sqrt_f32_e32 v2, v1
	s_nop 0
	v_add_u32_e32 v3, -1, v2
	v_fma_f32 v4, -v3, v2, v1
	v_cmp_ge_f32_e64 s[2:3], 0, v4
	v_add_u32_e32 v4, 1, v2
	s_nop 0
	v_cndmask_b32_e64 v3, v2, v3, s[2:3]
	v_fma_f32 v2, -v4, v2, v1
	v_cmp_lt_f32_e64 s[2:3], 0, v2
	s_nop 1
	v_cndmask_b32_e64 v2, v3, v4, s[2:3]
	v_mul_f32_e32 v3, 0x37800000, v2
	v_cndmask_b32_e64 v2, v2, v3, s[0:1]
	v_mov_b32_e32 v3, 0x260
	v_cmp_class_f32_e64 s[0:1], v1, v3
	s_nop 1
	v_cndmask_b32_e64 v1, v2, v1, s[0:1]
	v_sub_f32_e32 v1, 0x41f80000, v1
	v_mul_f32_e32 v1, 0.5, v1
	v_cvt_i32_f32_e32 v1, v1
	s_and_b64 s[0:1], exec, s[16:17]
	s_cselect_b32 s2, s40, s38
	s_cselect_b32 s3, s39, s33
	v_sub_u32_e32 v2, 31, v1
	v_mul_lo_u32 v2, v2, v1
	v_lshrrev_b32_e32 v3, 31, v2
	v_add_u32_e32 v2, v2, v3
	v_ashrrev_i32_e32 v2, 1, v2
	v_cmp_gt_i32_e64 s[0:1], v2, v0
	s_nop 1
	v_subbrev_co_u32_e64 v1, s[0:1], 0, v1, s[0:1]
	v_add_u32_e32 v2, 1, v1
	v_sub_u32_e32 v3, 30, v1
	v_mul_lo_u32 v3, v2, v3
	v_lshrrev_b32_e32 v4, 31, v3
	v_add_u32_e32 v3, v3, v4
	v_ashrrev_i32_e32 v3, 1, v3
	v_cmp_gt_i32_e64 s[0:1], v3, v0
	s_nop 1
	v_cndmask_b32_e64 v12, v2, v1, s[0:1]
	v_sub_u32_e32 v1, 31, v12
	v_mul_lo_u32 v1, v1, v12
	v_lshrrev_b32_e32 v2, 31, v1
	v_add_u32_e32 v1, v1, v2
	v_ashrrev_i32_e32 v1, 1, v1
	v_sub_u32_e32 v0, v0, v1
	v_cndmask_b32_e64 v1, 0, 16, vcc
	v_lshl_or_b32 v1, s2, 5, v1
	v_add_u32_e32 v1, v1, v12
	v_sub_u32_e32 v2, 0xff, v1
	v_mul_lo_u32 v1, v2, v1
	v_lshrrev_b32_e32 v2, 31, v1
	v_add_u32_e32 v1, v1, v2
	v_ashrrev_i32_e32 v1, 1, v1
	v_add3_u32 v13, v12, v0, 1
	v_add_u32_e32 v0, v1, v0
	v_ashrrev_i32_e32 v1, 31, v0
	v_mov_b32_e32 v2, 0x1fc0
	v_mad_u64_u32 v[0:1], s[0:1], s3, v2, v[0:1]
	v_mad_u64_u32 v[4:5], s[0:1], v0, 24, s[10:11]
	v_mov_b32_e32 v0, 0x17800
	v_lshl_add_u32 v14, v12, 2, v0
	v_mov_b32_e32 v0, 0x60
	v_cndmask_b32_e32 v15, 0, v0, vcc
	v_or_b32_e32 v2, 16, v15
	v_add_lshl_u32 v3, v2, v12, 6
	v_add_u32_e32 v2, v2, v13
	v_lshl_add_u32 v6, v2, 6, v14
	v_add_u32_e32 v2, 32, v15
	v_add_lshl_u32 v7, v2, v12, 6
	v_add_u32_e32 v2, v2, v13
	v_lshl_add_u32 v8, v2, 6, v14
	v_add_u32_e32 v2, 48, v15
	v_mad_i32_i24 v5, v1, 24, v5
	v_add_lshl_u32 v0, v15, v12, 6
	v_lshlrev_b32_e32 v16, 2, v13
	v_add_u32_e32 v1, v15, v13
	v_add_lshl_u32 v9, v2, v12, 6
	v_add_u32_e32 v17, 64, v15
	v_add_u32_e32 v15, 0x50, v15
	v_add3_u32 v0, v0, v16, s5
	v_lshl_add_u32 v1, v1, 6, v14
	v_add3_u32 v3, v3, v16, s5
	v_add3_u32 v7, v7, v16, s5
	v_add3_u32 v9, v9, v16, s5
	v_add_u32_e32 v2, v2, v13
	v_add_lshl_u32 v18, v17, v12, 6
	v_add_lshl_u32 v12, v15, v12, 6
	v_lshl_add_u32 v10, v2, 6, v14
	ds_read_b32 v0, v0
	ds_read_b32 v2, v1
	ds_read_b32 v1, v3
	ds_read_b32 v3, v6
	ds_read_b32 v6, v7
	ds_read_b32 v8, v8
	ds_read_b32 v7, v9
	ds_read_b32 v9, v10
	v_add3_u32 v18, v18, v16, s5
	v_add3_u32 v16, v12, v16, s5
	v_add_u32_e32 v12, v15, v13
	v_add_u32_e32 v17, v17, v13
	v_lshl_add_u32 v15, v12, 6, v14
	v_lshl_add_u32 v17, v17, 6, v14
	ds_read_b32 v12, v18
	ds_read_b32 v14, v17
	ds_read_b32 v13, v16
	ds_read_b32 v15, v15
	s_waitcnt lgkmcnt(0)
	v_pk_add_f32 v[0:1], v[0:1], v[2:3]
	v_mov_b32_e32 v2, s70
	v_mov_b32_e32 v3, s71
	v_mov_b64_e32 v[10:11], s[68:69]
	v_pk_add_f32 v[6:7], v[6:7], v[8:9]
	v_pk_fma_f32 v[0:1], v[0:1], s[4:5], v[10:11] op_sel_hi:[1,0,1]
	v_pk_fma_f32 v[2:3], v[6:7], s[4:5], v[2:3] op_sel_hi:[1,0,1]
	global_store_dwordx4 v[4:5], v[0:3], off
	s_nop 1
	v_pk_add_f32 v[0:1], v[12:13], v[14:15]
	v_mov_b64_e32 v[2:3], s[72:73]
	v_pk_fma_f32 v[0:1], v[0:1], s[4:5], v[2:3] op_sel_hi:[1,0,1]
	global_store_dwordx2 v[4:5], v[0:1], off offset:16
	s_endpgm
